# speedup vs baseline: 1.0126x; 1.0126x over previous
.LBB1_12:
	s_mov_b32 s0, s44
	s_add_i32 s44, s44, 1
	s_cmp_ge_u32 s44, s42
	s_cselect_b64 s[22:23], -1, 0
	s_cmp_lt_u32 s44, s42
	s_cselect_b32 s2, s44, s0
	s_waitcnt vmcnt(0)
	s_lshl_b32 s0, s2, 4
	s_mov_b32 s1, s17
	s_mov_b32 m0, s43
	ds_read_b128 v[76:79], v119 offset:32768
	ds_read_b128 v[80:83], v119 offset:36864
	ds_read_b128 v[84:87], v120 offset:32768
	ds_read_b128 v[88:91], v120 offset:36864
	ds_read_b128 v[92:95], v121
	ds_read_b128 v[96:99], v121 offset:4096
	ds_read_b128 v[128:131], v122
	ds_read_b128 v[132:135], v122 offset:4096
	ds_read_b128 v[72:75], v123
	s_waitcnt lgkmcnt(0)
	v_lshl_add_u64 v[70:71], s[0:1], 2, v[2:3]
	global_load_lds_dword v[70:71], off
	ds_read_b128 v[156:159], v115
	ds_read_b128 v[160:163], v115 offset:1024
	ds_read_b128 v[164:167], v115 offset:2048
	v_cvt_pk_bf16_f32 v136, v76, v77
	v_cvt_pk_bf16_f32 v137, v78, v79
	v_cvt_pk_bf16_f32 v138, v84, v85
	v_cvt_pk_bf16_f32 v139, v86, v87
	v_cvt_pk_bf16_f32 v140, v92, v93
	v_cvt_pk_bf16_f32 v141, v94, v95
	v_cvt_pk_bf16_f32 v142, v128, v129
	v_cvt_pk_bf16_f32 v143, v130, v131
	v_cvt_pk_bf16_f32 v144, v80, v81
	v_cvt_pk_bf16_f32 v145, v82, v83
	v_cvt_pk_bf16_f32 v146, v88, v89
	v_cvt_pk_bf16_f32 v147, v90, v91
	v_cvt_pk_bf16_f32 v128, v96, v97
	v_cvt_pk_bf16_f32 v129, v98, v99
	v_cvt_pk_bf16_f32 v130, v132, v133
	v_cvt_pk_bf16_f32 v131, v134, v135
	s_lshl_b32 s0, s2, 13
	s_cmp_lt_u32 s44, s42
	s_cselect_b32 s0, s0, 0x1e848000
	s_mov_b32 s61, s0
	s_add_i32 s63, s44, 1
	s_cmp_eq_u32 s63, s42
	s_cselect_b32 s63, 1, 0
	ds_read_b128 v[132:135], v115 offset:3072
	s_waitcnt lgkmcnt(3)
	v_mfma_f32_16x16x32_bf16 v[148:151], v[136:139], v[156:159], v[36:39]
	ds_read_b128 v[156:159], v115 offset:4096
	s_waitcnt lgkmcnt(3)
	v_mfma_f32_16x16x32_bf16 v[152:155], v[136:139], v[160:163], v[40:43]
	ds_read_b128 v[160:163], v115 offset:5120
	s_waitcnt lgkmcnt(3)
	v_mfma_f32_16x16x32_bf16 v[96:99], v[136:139], v[164:167], v[44:47]
	ds_read_b128 v[164:167], v115 offset:6144
	s_waitcnt lgkmcnt(3)
	v_mfma_f32_16x16x32_bf16 v[92:95], v[136:139], v[132:135], v[48:51]
	ds_read_b128 v[132:135], v115 offset:7168
	s_waitcnt lgkmcnt(3)
	v_mfma_f32_16x16x32_bf16 v[88:91], v[136:139], v[156:159], v[52:55]
	ds_read_b128 v[156:159], v115 offset:8192
	s_waitcnt lgkmcnt(3)
	v_mfma_f32_16x16x32_bf16 v[84:87], v[136:139], v[160:163], v[56:59]
	ds_read_b128 v[160:163], v115 offset:9216
	s_waitcnt lgkmcnt(3)
	v_mfma_f32_16x16x32_bf16 v[80:83], v[136:139], v[164:167], v[60:63]
	ds_read_b128 v[164:167], v115 offset:10240
	s_waitcnt lgkmcnt(3)
	v_mfma_f32_16x16x32_bf16 v[76:79], v[136:139], v[132:135], v[64:67]
	ds_read_b128 v[132:135], v115 offset:11264
	s_waitcnt lgkmcnt(3)
	v_mfma_f32_16x16x32_bf16 v[148:151], v[140:143], v[156:159], v[148:151]
	ds_read_b128 v[156:159], v115 offset:12288
	s_waitcnt lgkmcnt(3)
	v_mfma_f32_16x16x32_bf16 v[152:155], v[140:143], v[160:163], v[152:155]
	ds_read_b128 v[160:163], v115 offset:13312
	s_waitcnt lgkmcnt(3)
	v_mfma_f32_16x16x32_bf16 v[96:99], v[140:143], v[164:167], v[96:99]
	ds_read_b128 v[164:167], v115 offset:14336
	s_waitcnt lgkmcnt(3)
	v_mfma_f32_16x16x32_bf16 v[92:95], v[140:143], v[132:135], v[92:95]
	ds_read_b128 v[132:135], v115 offset:15360
	s_waitcnt lgkmcnt(3)
	v_mfma_f32_16x16x32_bf16 v[88:91], v[140:143], v[156:159], v[88:91]
	ds_read_b128 v[156:159], v115 offset:16384
	s_waitcnt lgkmcnt(3)
	v_mfma_f32_16x16x32_bf16 v[84:87], v[140:143], v[160:163], v[84:87]
	ds_read_b128 v[160:163], v115 offset:17408
	s_waitcnt lgkmcnt(3)
	v_mfma_f32_16x16x32_bf16 v[80:83], v[140:143], v[164:167], v[80:83]
	ds_read_b128 v[164:167], v115 offset:18432
	s_waitcnt lgkmcnt(3)
	v_mfma_f32_16x16x32_bf16 v[76:79], v[140:143], v[132:135], v[76:79]
	ds_read_b128 v[132:135], v115 offset:19456
	s_waitcnt lgkmcnt(3)
	s_mov_b32 m0, s47
	s_nop 0
	buffer_load_dwordx4 v113, s[12:15], s61 offen nt lds
	s_cmp_eq_u32 s63, 0
	s_cbranch_scc1 .Lmain_noburst
	s_or_b32 s62, s61, 0x800
	s_mov_b32 m0, s48
	s_nop 0
	buffer_load_dwordx4 v113, s[12:15], s62 offen nt lds
	s_or_b32 s62, s61, 0x1000
	s_mov_b32 m0, s49
	s_nop 0
	buffer_load_dwordx4 v113, s[12:15], s62 offen nt lds
	s_or_b32 s62, s61, 0x1800
	s_mov_b32 m0, s50
	s_nop 0
	buffer_load_dwordx4 v113, s[12:15], s62 offen nt lds
	s_or_b32 s62, s61, 0x100
	s_mov_b32 m0, s51
	s_nop 0
	buffer_load_dwordx4 v113, s[12:15], s62 offen nt lds
	s_or_b32 s62, s61, 0x900
	s_mov_b32 m0, s52
	s_nop 0
	buffer_load_dwordx4 v113, s[12:15], s62 offen nt lds
	s_or_b32 s62, s61, 0x1100
	s_mov_b32 m0, s53
	s_nop 0
	buffer_load_dwordx4 v113, s[12:15], s62 offen nt lds
	s_or_b32 s62, s61, 0x1900
	s_mov_b32 m0, s54
	s_nop 0
	buffer_load_dwordx4 v113, s[12:15], s62 offen nt lds
.Lmain_noburst:
	v_mfma_f32_16x16x32_bf16 v[148:151], v[144:147], v[156:159], v[148:151]
	ds_read_b128 v[156:159], v115 offset:20480
	s_waitcnt lgkmcnt(3)
	v_mfma_f32_16x16x32_bf16 v[152:155], v[144:147], v[160:163], v[152:155]
	ds_read_b128 v[160:163], v115 offset:21504
	s_waitcnt lgkmcnt(3)
	v_mfma_f32_16x16x32_bf16 v[96:99], v[144:147], v[164:167], v[96:99]
	ds_read_b128 v[164:167], v115 offset:22528
	s_waitcnt lgkmcnt(3)
	v_mfma_f32_16x16x32_bf16 v[92:95], v[144:147], v[132:135], v[92:95]
	ds_read_b128 v[132:135], v115 offset:23552
	s_waitcnt lgkmcnt(3)
	v_mfma_f32_16x16x32_bf16 v[88:91], v[144:147], v[156:159], v[88:91]
	ds_read_b128 v[156:159], v115 offset:24576
	s_waitcnt lgkmcnt(3)
	v_mfma_f32_16x16x32_bf16 v[84:87], v[144:147], v[160:163], v[84:87]
	ds_read_b128 v[160:163], v115 offset:25600
	s_waitcnt lgkmcnt(3)
	v_mfma_f32_16x16x32_bf16 v[80:83], v[144:147], v[164:167], v[80:83]
	ds_read_b128 v[164:167], v115 offset:26624
	s_waitcnt lgkmcnt(3)
	v_mfma_f32_16x16x32_bf16 v[76:79], v[144:147], v[132:135], v[76:79]
	ds_read_b128 v[132:135], v115 offset:27648
	s_waitcnt lgkmcnt(3)
	v_mfma_f32_16x16x32_bf16 v[148:151], v[128:131], v[156:159], v[148:151]
	ds_read_b128 v[156:159], v115 offset:28672
	s_waitcnt lgkmcnt(3)
	v_mfma_f32_16x16x32_bf16 v[152:155], v[128:131], v[160:163], v[152:155]
	ds_read_b128 v[160:163], v115 offset:29696
	s_waitcnt lgkmcnt(3)
	v_mfma_f32_16x16x32_bf16 v[96:99], v[128:131], v[164:167], v[96:99]
	ds_read_b128 v[164:167], v115 offset:30720
	s_waitcnt lgkmcnt(3)
	v_mfma_f32_16x16x32_bf16 v[92:95], v[128:131], v[132:135], v[92:95]
	ds_read_b128 v[132:135], v115 offset:31744
	s_waitcnt lgkmcnt(3)
	v_mfma_f32_16x16x32_bf16 v[88:91], v[128:131], v[156:159], v[88:91]
	s_waitcnt lgkmcnt(2)
	v_mfma_f32_16x16x32_bf16 v[84:87], v[128:131], v[160:163], v[84:87]
	s_waitcnt lgkmcnt(1)
	v_mfma_f32_16x16x32_bf16 v[80:83], v[128:131], v[164:167], v[80:83]
	s_waitcnt lgkmcnt(0)
	v_mfma_f32_16x16x32_bf16 v[76:79], v[128:131], v[132:135], v[76:79]
	s_cmp_lg_u32 s63, 0
	s_cbranch_scc1 .Lmain_skip1
	s_or_b32 s62, s61, 0x800
	s_mov_b32 m0, s48
	s_nop 0
	buffer_load_dwordx4 v113, s[12:15], s62 offen nt lds
.Lmain_skip1:
	ds_read2_b32 v[136:137], v114 offset0:128 offset1:144
	ds_read2_b32 v[138:139], v125 offset1:16
	ds_read2_b32 v[140:141], v114 offset0:160 offset1:176
	ds_read2_b32 v[142:143], v125 offset0:32 offset1:48
	ds_read2_b32 v[144:145], v114 offset0:192 offset1:208
	ds_read2_b32 v[146:147], v125 offset0:64 offset1:80
	ds_read2_b32 v[156:157], v114 offset0:224 offset1:240
	ds_read2_b32 v[158:159], v125 offset0:96 offset1:112
	v_fma_f32 v70, v149, v149, 0
	v_fmac_f32_e32 v70, v153, v153
	v_fmac_f32_e32 v70, v97, v97
	v_fmac_f32_e32 v70, v93, v93
	v_fmac_f32_e32 v70, v89, v89
	v_fmac_f32_e32 v70, v85, v85
	v_fmac_f32_e32 v70, v81, v81
	v_fmac_f32_e32 v70, v77, v77
	v_fma_f32 v68, v148, v148, 0
	v_fmac_f32_e32 v68, v152, v152
	v_add_f32_dpp v70, v70, v70 quad_perm:[1,0,3,2] row_mask:0xf bank_mask:0xf bound_ctrl:1
	v_fmac_f32_e32 v68, v96, v96
	v_fmac_f32_e32 v68, v92, v92
	v_add_f32_dpp v70, v70, v70 quad_perm:[2,3,0,1] row_mask:0xf bank_mask:0xf bound_ctrl:1
	v_fmac_f32_e32 v68, v88, v88
	v_fmac_f32_e32 v68, v84, v84
	v_add_f32_dpp v70, v70, v70 row_half_mirror row_mask:0xf bank_mask:0xf bound_ctrl:1
	v_fmac_f32_e32 v68, v80, v80
	v_fmac_f32_e32 v68, v76, v76
	v_add_f32_dpp v70, v70, v70 row_mirror row_mask:0xf bank_mask:0xf bound_ctrl:1
	v_fmamk_f32 v70, v70, 0x3c000000, v124
	s_cmp_lg_u32 s63, 0
	s_cbranch_scc1 .Lmain_skip2
	s_or_b32 s62, s61, 0x1000
	s_mov_b32 m0, s49
	s_nop 0
	buffer_load_dwordx4 v113, s[12:15], s62 offen nt lds
.Lmain_skip2:
	v_rsq_f32_e32 v127, v70
	v_fma_f32 v70, v150, v150, 0
	v_fmac_f32_e32 v70, v154, v154
	v_fmac_f32_e32 v70, v98, v98
	v_fmac_f32_e32 v70, v94, v94
	v_fmac_f32_e32 v70, v90, v90
	v_fmac_f32_e32 v70, v86, v86
	v_fmac_f32_e32 v70, v82, v82
	v_fmac_f32_e32 v70, v78, v78
	v_add_f32_dpp v68, v68, v68 quad_perm:[1,0,3,2] row_mask:0xf bank_mask:0xf bound_ctrl:1
	v_mul_f32_e32 v131, v127, v149
	v_add_f32_dpp v70, v70, v70 quad_perm:[1,0,3,2] row_mask:0xf bank_mask:0xf bound_ctrl:1
	v_add_f32_dpp v68, v68, v68 quad_perm:[2,3,0,1] row_mask:0xf bank_mask:0xf bound_ctrl:1
	v_mul_f32_e32 v81, v127, v81
	v_add_f32_dpp v70, v70, v70 quad_perm:[2,3,0,1] row_mask:0xf bank_mask:0xf bound_ctrl:1
	v_add_f32_dpp v68, v68, v68 row_half_mirror row_mask:0xf bank_mask:0xf bound_ctrl:1
	v_cmp_gt_u32_e64 s[0:1], s55, v72
	v_add_f32_dpp v70, v70, v70 row_half_mirror row_mask:0xf bank_mask:0xf bound_ctrl:1
	v_add_f32_dpp v68, v68, v68 row_mirror row_mask:0xf bank_mask:0xf bound_ctrl:1
	v_fmamk_f32 v68, v68, 0x3c000000, v124
	v_add_f32_dpp v70, v70, v70 row_mirror row_mask:0xf bank_mask:0xf bound_ctrl:1
	v_fmamk_f32 v70, v70, 0x3c000000, v124
	v_rsq_f32_e32 v130, v70
	v_fma_f32 v70, v151, v151, 0
	v_fmac_f32_e32 v70, v155, v155
	v_fmac_f32_e32 v70, v99, v99
	v_fmac_f32_e32 v70, v95, v95
	v_fmac_f32_e32 v70, v91, v91
	v_fmac_f32_e32 v70, v87, v87
	v_fmac_f32_e32 v70, v83, v83
	v_fmac_f32_e32 v70, v79, v79
	v_rsq_f32_e32 v68, v68
	v_mul_f32_e32 v98, v130, v98
	v_add_f32_dpp v70, v70, v70 quad_perm:[1,0,3,2] row_mask:0xf bank_mask:0xf bound_ctrl:1
	v_mul_f32_e32 v90, v130, v90
	v_mul_f32_e32 v111, v68, v148
	v_add_f32_dpp v110, v70, v70 quad_perm:[2,3,0,1] row_mask:0xf bank_mask:0xf bound_ctrl:1
	s_nop 1
	v_add_f32_dpp v110, v110, v110 row_half_mirror row_mask:0xf bank_mask:0xf bound_ctrl:1
	v_mul_f32_e32 v96, v68, v96
	v_mul_f32_e32 v92, v68, v92
	v_add_f32_dpp v110, v110, v110 row_mirror row_mask:0xf bank_mask:0xf bound_ctrl:1
	v_fmamk_f32 v110, v110, 0x3c000000, v124
	s_waitcnt lgkmcnt(0)
	s_cmp_lg_u32 s63, 0
	s_cbranch_scc1 .Lmain_skip3
	s_or_b32 s62, s61, 0x1800
	s_mov_b32 m0, s50
	s_nop 0
	buffer_load_dwordx4 v113, s[12:15], s62 offen nt lds
.Lmain_skip3:
	v_fma_f32 v111, v111, v136, v138
	v_fma_f32 v131, v131, v136, v138
	v_exp_f32_e32 v111, v111
	v_exp_f32_e32 v131, v131
	v_rsq_f32_e32 v132, v110
	v_mul_f32_e32 v88, v68, v88
	v_add_f32_e32 v110, 1.0, v111
	v_add_f32_e32 v111, 1.0, v131
	v_mul_f32_e32 v131, v130, v150
	v_mul_f32_e32 v133, v132, v151
	v_fma_f32 v131, v131, v136, v138
	v_fma_f32 v70, v133, v136, v138
	v_exp_f32_e32 v131, v131
	v_exp_f32_e32 v70, v70
	v_rcp_f32_e32 v110, v110
	v_rcp_f32_e32 v111, v111
	v_add_f32_e32 v128, 1.0, v131
	v_add_f32_e32 v70, 1.0, v70
	v_rcp_f32_e32 v128, v128
	v_rcp_f32_e32 v70, v70
	v_mul_f32_e32 v131, v68, v152
	v_fma_f32 v131, v131, v137, v139
	v_cvt_pk_bf16_f32 v110, v110, v111
	v_cvt_pk_bf16_f32 v111, v128, v70
	v_mul_f32_e32 v128, v127, v153
	v_exp_f32_e32 v131, v131
	v_fma_f32 v128, v128, v137, v139
	v_exp_f32_e32 v128, v128
	v_mul_f32_e32 v99, v132, v99
	v_add_f32_e32 v70, 1.0, v131
	v_rcp_f32_e32 v133, v70
	v_add_f32_e32 v70, 1.0, v128
	v_mul_f32_e32 v131, v130, v154
	v_rcp_f32_e32 v134, v70
	v_mul_f32_e32 v70, v132, v155
	v_fma_f32 v131, v131, v137, v139
	v_fma_f32 v129, v70, v137, v139
	v_exp_f32_e32 v135, v129
	v_exp_f32_e32 v131, v131
	v_mul_f32_e32 v91, v132, v91
	v_add_f32_e32 v135, 1.0, v135
	v_rcp_f32_e32 v135, v135
	s_cmp_lg_u32 s63, 0
	s_cbranch_scc1 .Lmain_skip4
	s_or_b32 s62, s61, 0x100
	s_mov_b32 m0, s51
	s_nop 0
	buffer_load_dwordx4 v113, s[12:15], s62 offen nt lds
.Lmain_skip4:
	v_fma_f32 v96, v96, v140, v142
	v_exp_f32_e32 v136, v96
	v_mul_f32_e32 v96, v127, v97
	v_fma_f32 v96, v96, v140, v142
	v_exp_f32_e32 v97, v96
	v_fma_f32 v98, v98, v140, v142
	v_fma_f32 v70, v99, v140, v142
	v_exp_f32_e32 v98, v98
	v_exp_f32_e32 v70, v70
	v_add_f32_e32 v97, 1.0, v97
	v_cvt_pk_bf16_f32 v96, v133, v134
	v_add_f32_e32 v133, 1.0, v136
	v_rcp_f32_e32 v99, v97
	v_add_f32_e32 v97, 1.0, v98
	v_add_f32_e32 v70, 1.0, v70
	v_fma_f32 v92, v92, v141, v143
	v_rcp_f32_e32 v133, v133
	v_rcp_f32_e32 v128, v97
	v_rcp_f32_e32 v70, v70
	v_exp_f32_e32 v92, v92
	v_cvt_pk_bf16_f32 v98, v133, v99
	v_add_f32_e32 v131, 1.0, v131
	v_cvt_pk_bf16_f32 v99, v128, v70
	v_add_f32_e32 v70, 1.0, v92
	v_mul_f32_e32 v92, v127, v93
	v_fma_f32 v92, v92, v141, v143
	v_exp_f32_e32 v92, v92
	v_mul_f32_e32 v93, v130, v94
	v_fma_f32 v93, v93, v141, v143
	v_rcp_f32_e32 v131, v131
	v_exp_f32_e32 v93, v93
	v_rcp_f32_e32 v94, v70
	v_add_f32_e32 v70, 1.0, v92
	v_rcp_f32_e32 v128, v70
	v_mul_f32_e32 v70, v132, v95
	v_cvt_pk_bf16_f32 v97, v131, v135
	v_add_f32_e32 v131, 1.0, v93
	v_fma_f32 v129, v70, v141, v143
	v_exp_f32_e32 v95, v129
	v_rcp_f32_e32 v129, v131
	v_mul_f32_e32 v84, v68, v84
	v_mul_f32_e32 v80, v68, v80
	s_cmp_lg_u32 s63, 0
	s_cbranch_scc1 .Lmain_skip5
	s_or_b32 s62, s61, 0x900
	s_mov_b32 m0, s52
	s_nop 0
	buffer_load_dwordx4 v113, s[12:15], s62 offen nt lds
.Lmain_skip5:
	v_fma_f32 v88, v88, v144, v146
	v_exp_f32_e32 v131, v88
	v_mul_f32_e32 v88, v127, v89
	v_fma_f32 v88, v88, v144, v146
	v_exp_f32_e32 v89, v88
	v_fma_f32 v90, v90, v144, v146
	v_fma_f32 v70, v91, v144, v146
	v_exp_f32_e32 v90, v90
	v_exp_f32_e32 v70, v70
	v_add_f32_e32 v89, 1.0, v89
	v_cvt_pk_bf16_f32 v88, v94, v128
	v_add_f32_e32 v94, 1.0, v131
	v_rcp_f32_e32 v91, v89
	v_add_f32_e32 v89, 1.0, v90
	v_add_f32_e32 v70, 1.0, v70
	v_fma_f32 v84, v84, v145, v147
	v_rcp_f32_e32 v94, v94
	v_rcp_f32_e32 v92, v89
	v_rcp_f32_e32 v70, v70
	v_exp_f32_e32 v84, v84
	v_cvt_pk_bf16_f32 v90, v94, v91
	v_mul_f32_e32 v68, v68, v76
	v_cvt_pk_bf16_f32 v91, v92, v70
	v_add_f32_e32 v70, 1.0, v84
	v_mul_f32_e32 v84, v127, v85
	v_fma_f32 v84, v84, v145, v147
	v_mul_f32_e32 v85, v130, v86
	v_exp_f32_e32 v84, v84
	v_fma_f32 v85, v85, v145, v147
	v_exp_f32_e32 v85, v85
	v_rcp_f32_e32 v92, v70
	v_add_f32_e32 v70, 1.0, v84
	v_rcp_f32_e32 v84, v70
	v_add_f32_e32 v70, 1.0, v85
	v_mul_f32_e32 v85, v132, v87
	v_fma_f32 v93, v85, v145, v147
	v_exp_f32_e32 v85, v93
	v_rcp_f32_e32 v93, v70
	v_mul_f32_e32 v76, v127, v77
	v_mul_f32_e32 v82, v130, v82
	v_mul_f32_e32 v83, v132, v83
	v_mul_f32_e32 v77, v130, v78
	s_cmp_lg_u32 s63, 0
	s_cbranch_scc1 .Lmain_skip6
	s_or_b32 s62, s61, 0x1100
	s_mov_b32 m0, s53
	s_nop 0
	buffer_load_dwordx4 v113, s[12:15], s62 offen nt lds
.Lmain_skip6:
	v_fma_f32 v76, v76, v157, v159
	v_mul_f32_e32 v78, v132, v79
	v_fma_f32 v80, v80, v156, v158
	v_fma_f32 v81, v81, v156, v158
	v_fma_f32 v82, v82, v156, v158
	v_fma_f32 v70, v83, v156, v158
	v_fma_f32 v68, v68, v157, v159
	v_exp_f32_e32 v76, v76
	v_fma_f32 v77, v77, v157, v159
	v_fma_f32 v87, v78, v157, v159
	v_exp_f32_e32 v82, v82
	v_exp_f32_e32 v70, v70
	v_exp_f32_e32 v68, v68
	v_exp_f32_e32 v77, v77
	v_exp_f32_e32 v71, v87
	v_add_f32_e32 v76, 1.0, v76
	v_add_f32_e32 v82, 1.0, v82
	v_add_f32_e32 v70, 1.0, v70
	v_add_f32_e32 v68, 1.0, v68
	v_rcp_f32_e32 v78, v76
	v_add_f32_e32 v76, 1.0, v77
	v_add_f32_e32 v71, 1.0, v71
	v_rcp_f32_e32 v82, v82
	v_rcp_f32_e32 v70, v70
	v_rcp_f32_e32 v68, v68
	v_rcp_f32_e32 v79, v76
	v_rcp_f32_e32 v71, v71
	v_exp_f32_e32 v80, v80
	v_exp_f32_e32 v81, v81
	v_cvt_pk_bf16_f32 v77, v82, v70
	v_cvt_pk_bf16_f32 v78, v68, v78
	v_cvt_pk_bf16_f32 v79, v79, v71
	v_subrev_u32_e32 v68, s16, v72
	v_subrev_u32_e32 v70, s16, v73
	v_subrev_u32_e32 v71, s16, v74
	v_add_f32_e32 v95, 1.0, v95
	v_add_f32_e32 v85, 1.0, v85
	v_add_f32_e32 v80, 1.0, v80
	v_add_f32_e32 v81, 1.0, v81
	s_cmp_lg_u32 s63, 0
	s_cbranch_scc1 .Lmain_skip7
	s_or_b32 s62, s61, 0x1900
	s_mov_b32 m0, s54
	s_nop 0
	buffer_load_dwordx4 v113, s[12:15], s62 offen nt lds
.Lmain_skip7:
	v_max3_u32 v68, v68, v70, v71
	v_subrev_u32_e32 v70, s16, v75
	v_rcp_f32_e32 v95, v95
	v_rcp_f32_e32 v85, v85
	v_rcp_f32_e32 v80, v80
	v_rcp_f32_e32 v81, v81
	v_max_u32_e32 v68, v68, v70
	v_cmp_gt_u32_e32 vcc, 16, v68
	s_cmp_eq_u64 vcc, -1
	s_cselect_b64 s[24:25], -1, 0
	s_cmp_lg_u64 vcc, -1
	v_cvt_pk_bf16_f32 v89, v129, v95
	v_cvt_pk_bf16_f32 v84, v92, v84
	v_cvt_pk_bf16_f32 v85, v93, v85
	v_cvt_pk_bf16_f32 v76, v80, v81
	s_cselect_b64 s[26:27], -1, 0
	v_cmp_gt_u32_e64 s[2:3], s55, v73
	v_cmp_gt_u32_e64 s[4:5], s55, v74
	v_cmp_gt_u32_e64 s[6:7], s55, v75
	s_mov_b32 s8, 0
	s_branch .LBB1_14
